# grid barrier spin loops poll back-to-back (s_sleep 1 between polls removed)
# speedup vs baseline: 1.0006x; 1.0006x over previous
; __device__ __forceinline__ unsigned xb_ld(unsigned* p)              { unsigned GAS* g = (unsigned GAS*)p; asm volatile("" : "+s"(g)); return __hip_atomic_load(g, __ATOMIC_RELAXED, __HIP_MEMORY_SCOPE_AGENT); }
; __device__ __forceinline__ unsigned xb_add(unsigned* p, unsigned v) { unsigned GAS* g = (unsigned GAS*)p; asm volatile("" : "+s"(g)); return __hip_atomic_fetch_add(g, v, __ATOMIC_RELAXED, __HIP_MEMORY_SCOPE_AGENT); }
; __device__ __forceinline__ void xcd_barrier_complete(unsigned* bar, unsigned x, unsigned& nloc, unsigned& nx) {
;     ...
;     for (;;) {
;         sum = 0u; cnt = 0u;
; #pragma unroll 1
;         for (unsigned j = 0; j < 16; ++j) { const unsigned c = xb_ld(&bar[XB_XCNT(j)]); sum += c; cnt += (c > 0u) ? 1u : 0u; }
;         if (sum == G) break;
;         __builtin_amdgcn_s_sleep(1);
;         if ((++sp & 255u) == 0u) { if (xb_ld(&bar[XB_TMO])) break; if (sp > XB_SPIN_CAP) { (void)xb_add(&bar[XB_TMO], 1u); break; } }
;     }
.LBB0_162:
	s_add_u32 s10, s16, s8
	s_addc_u32 s11, s18, s9
	global_load_dword v3, v1, s[10:11] sc1
	s_waitcnt vmcnt(0)
	v_cmp_ne_u32_e32 vcc, 0, v3
	s_cmp_lg_u64 vcc, 0
	s_addc_u32 s15, s15, 0
	s_add_u32 s8, s8, 0x100
	s_addc_u32 s9, s9, 0
	s_cmpk_eq_i32 s8, 0x1000
	v_add_u32_e32 v2, v3, v2
	s_cbranch_scc0 .LBB0_162
	v_cmp_ne_u32_e32 vcc, s17, v2
	s_mov_b64 s[8:9], -1
	s_mov_b64 s[10:11], -1
	s_cbranch_vccz .LBB0_160
	s_add_i32 s19, s19, 1
	s_and_b32 s10, s19, 0xff
	s_cmp_eq_u32 s10, 0
	s_cselect_b64 s[10:11], -1, 0
	s_and_b64 vcc, exec, s[10:11]
	s_nop 0
	s_cbranch_vccz .LBB0_160
	s_mov_b64 s[8:9], s[6:7]
	global_load_dword v2, v1, s[8:9] sc1
	s_mov_b64 s[8:9], -1
	s_waitcnt vmcnt(0)
	v_cmp_eq_u32_e32 vcc, 0, v2
	s_cbranch_vccz .LBB0_160
	s_cmp_gt_u32 s19, 0x40000
	s_mov_b64 s[8:9], 0
	s_cselect_b64 s[10:11], -1, 0
	s_branch .LBB0_160

; __device__ __forceinline__ unsigned xb_ld(unsigned* p)              { unsigned GAS* g = (unsigned GAS*)p; asm volatile("" : "+s"(g)); return __hip_atomic_load(g, __ATOMIC_RELAXED, __HIP_MEMORY_SCOPE_AGENT); }
; #define XB_SPIN(cond, bar) do { unsigned _sp = 0; while (cond) { __builtin_amdgcn_s_sleep(1); \
;     if ((++_sp & 255u) == 0u) { if (xb_ld(&(bar)[XB_TMO])) break; if (_sp > XB_SPIN_CAP) { (void)xb_add(&(bar)[XB_TMO], 1u); break; } } } } while (0)
; __device__ __forceinline__ void xcd_barrier(const XcdBarrier& b) {
;     ...
;             XB_SPIN(xb_ld(&bar[XB_XGEN(b.x)]) == gen, bar);
.LBB0_178:
	s_mov_b64 s[20:21], s[10:11]
	global_load_dword v3, v1, s[20:21] sc1
	s_or_b64 s[18:19], s[18:19], exec
	s_or_b64 s[16:17], s[16:17], exec
	s_waitcnt vmcnt(0)
	v_cmp_eq_u32_e32 vcc, v3, v2
	s_and_saveexec_b64 s[20:21], vcc
	s_cbranch_execz .LBB0_177
	s_and_b32 s24, s30, 0xff
	s_mov_b64 s[22:23], -1
	s_cmp_eq_u32 s24, 0
	s_mov_b64 s[24:25], -1
	s_mov_b64 s[26:27], -1
	s_nop 0
	s_cbranch_scc1 .LBB0_182
	s_and_b64 vcc, exec, s[26:27]
	s_cbranch_vccz .LBB0_176

; __device__ __forceinline__ unsigned xb_ld(unsigned* p)              { unsigned GAS* g = (unsigned GAS*)p; asm volatile("" : "+s"(g)); return __hip_atomic_load(g, __ATOMIC_RELAXED, __HIP_MEMORY_SCOPE_AGENT); }
; #define XB_SPIN(cond, bar) do { unsigned _sp = 0; while (cond) { __builtin_amdgcn_s_sleep(1); \
;     if ((++_sp & 255u) == 0u) { if (xb_ld(&(bar)[XB_TMO])) break; if (_sp > XB_SPIN_CAP) { (void)xb_add(&(bar)[XB_TMO], 1u); break; } } } } while (0)
; __device__ __forceinline__ void xcd_barrier(const XcdBarrier& b) {
;     ...
;             else XB_SPIN(xb_ld(&bar[XB_TOPGEN]) == tg, bar);
.LBB0_197:
	s_mov_b64 s[18:19], s[6:7]
	global_load_dword v3, v1, s[18:19] sc1
	s_or_b64 s[16:17], s[16:17], exec
	s_or_b64 s[14:15], s[14:15], exec
	s_waitcnt vmcnt(0)
	v_cmp_eq_u32_e32 vcc, v3, v2
	s_and_saveexec_b64 s[18:19], vcc
	s_cbranch_execz .LBB0_196
	s_and_b32 s22, s26, 0xff
	s_mov_b64 s[20:21], -1
	s_cmp_eq_u32 s22, 0
	s_mov_b64 s[22:23], -1
	s_mov_b64 s[24:25], -1
	s_nop 0
	s_cbranch_scc1 .LBB0_201
	s_and_b64 vcc, exec, s[24:25]
	s_cbranch_vccz .LBB0_195

; __device__ __forceinline__ unsigned xb_ld(unsigned* p)              { unsigned GAS* g = (unsigned GAS*)p; asm volatile("" : "+s"(g)); return __hip_atomic_load(g, __ATOMIC_RELAXED, __HIP_MEMORY_SCOPE_AGENT); }
; __device__ __forceinline__ unsigned xb_add(unsigned* p, unsigned v) { unsigned GAS* g = (unsigned GAS*)p; asm volatile("" : "+s"(g)); return __hip_atomic_fetch_add(g, v, __ATOMIC_RELAXED, __HIP_MEMORY_SCOPE_AGENT); }
; __device__ __forceinline__ void xcd_barrier_complete(unsigned* bar, unsigned x, unsigned& nloc, unsigned& nx) {
;     ...
;     for (;;) {
;         sum = 0u; cnt = 0u;
; #pragma unroll 1
;         for (unsigned j = 0; j < 16; ++j) { const unsigned c = xb_ld(&bar[XB_XCNT(j)]); sum += c; cnt += (c > 0u) ? 1u : 0u; }
;         if (sum == G) break;
;         __builtin_amdgcn_s_sleep(1);
;         if ((++sp & 255u) == 0u) { if (xb_ld(&bar[XB_TMO])) break; if (sp > XB_SPIN_CAP) { (void)xb_add(&bar[XB_TMO], 1u); break; } }
;     }
.LBB0_239:
	s_add_u32 s8, s14, s6
	s_addc_u32 s9, s16, s7
	global_load_dword v3, v1, s[8:9] sc1
	s_waitcnt vmcnt(0)
	v_cmp_ne_u32_e32 vcc, 0, v3
	s_cmp_lg_u64 vcc, 0
	s_addc_u32 s13, s13, 0
	s_add_u32 s6, s6, 0x100
	s_addc_u32 s7, s7, 0
	s_cmpk_eq_i32 s6, 0x1000
	v_add_u32_e32 v2, v3, v2
	s_cbranch_scc0 .LBB0_239
	v_cmp_ne_u32_e32 vcc, s15, v2
	s_mov_b64 s[6:7], -1
	s_mov_b64 s[8:9], -1
	s_cbranch_vccz .LBB0_237
	s_add_i32 s17, s17, 1
	s_and_b32 s8, s17, 0xff
	s_cmp_eq_u32 s8, 0
	s_cselect_b64 s[8:9], -1, 0
	s_and_b64 vcc, exec, s[8:9]
	s_nop 0
	s_cbranch_vccz .LBB0_237
	s_mov_b64 s[6:7], s[4:5]
	global_load_dword v2, v1, s[6:7] sc1
	s_mov_b64 s[6:7], -1
	s_waitcnt vmcnt(0)
	v_cmp_eq_u32_e32 vcc, 0, v2
	s_cbranch_vccz .LBB0_237
	s_cmp_gt_u32 s17, 0x40000
	s_mov_b64 s[6:7], 0
	s_cselect_b64 s[8:9], -1, 0
	s_branch .LBB0_237

; __device__ __forceinline__ unsigned xb_ld(unsigned* p)              { unsigned GAS* g = (unsigned GAS*)p; asm volatile("" : "+s"(g)); return __hip_atomic_load(g, __ATOMIC_RELAXED, __HIP_MEMORY_SCOPE_AGENT); }
; #define XB_SPIN(cond, bar) do { unsigned _sp = 0; while (cond) { __builtin_amdgcn_s_sleep(1); \
;     if ((++_sp & 255u) == 0u) { if (xb_ld(&(bar)[XB_TMO])) break; if (_sp > XB_SPIN_CAP) { (void)xb_add(&(bar)[XB_TMO], 1u); break; } } } } while (0)
; __device__ __forceinline__ void xcd_barrier(const XcdBarrier& b) {
;     ...
;             XB_SPIN(xb_ld(&bar[XB_XGEN(b.x)]) == gen, bar);
.LBB0_255:
	s_mov_b64 s[18:19], s[8:9]
	global_load_dword v3, v1, s[18:19] sc1
	s_or_b64 s[16:17], s[16:17], exec
	s_or_b64 s[14:15], s[14:15], exec
	s_waitcnt vmcnt(0)
	v_cmp_eq_u32_e32 vcc, v3, v2
	s_and_saveexec_b64 s[18:19], vcc
	s_cbranch_execz .LBB0_254
	s_and_b32 s22, s28, 0xff
	s_mov_b64 s[20:21], -1
	s_cmp_eq_u32 s22, 0
	s_mov_b64 s[22:23], -1
	s_mov_b64 s[24:25], -1
	s_nop 0
	s_cbranch_scc1 .LBB0_259
	s_and_b64 vcc, exec, s[24:25]
	s_cbranch_vccz .LBB0_253

; __device__ __forceinline__ unsigned xb_ld(unsigned* p)              { unsigned GAS* g = (unsigned GAS*)p; asm volatile("" : "+s"(g)); return __hip_atomic_load(g, __ATOMIC_RELAXED, __HIP_MEMORY_SCOPE_AGENT); }
; #define XB_SPIN(cond, bar) do { unsigned _sp = 0; while (cond) { __builtin_amdgcn_s_sleep(1); \
;     if ((++_sp & 255u) == 0u) { if (xb_ld(&(bar)[XB_TMO])) break; if (_sp > XB_SPIN_CAP) { (void)xb_add(&(bar)[XB_TMO], 1u); break; } } } } while (0)
; __device__ __forceinline__ void xcd_barrier(const XcdBarrier& b) {
;     ...
;             else XB_SPIN(xb_ld(&bar[XB_TOPGEN]) == tg, bar);
.LBB0_274:
	s_mov_b64 s[16:17], s[4:5]
	global_load_dword v3, v1, s[16:17] sc1
	s_or_b64 s[14:15], s[14:15], exec
	s_or_b64 s[12:13], s[12:13], exec
	s_waitcnt vmcnt(0)
	v_cmp_eq_u32_e32 vcc, v3, v2
	s_and_saveexec_b64 s[16:17], vcc
	s_cbranch_execz .LBB0_273
	s_and_b32 s20, s24, 0xff
	s_mov_b64 s[18:19], -1
	s_cmp_eq_u32 s20, 0
	s_mov_b64 s[20:21], -1
	s_mov_b64 s[22:23], -1
	s_nop 0
	s_cbranch_scc1 .LBB0_278
	s_and_b64 vcc, exec, s[22:23]
	s_cbranch_vccz .LBB0_272

; __device__ __forceinline__ unsigned xb_ld(unsigned* p)              { unsigned GAS* g = (unsigned GAS*)p; asm volatile("" : "+s"(g)); return __hip_atomic_load(g, __ATOMIC_RELAXED, __HIP_MEMORY_SCOPE_AGENT); }
; __device__ __forceinline__ unsigned xb_add(unsigned* p, unsigned v) { unsigned GAS* g = (unsigned GAS*)p; asm volatile("" : "+s"(g)); return __hip_atomic_fetch_add(g, v, __ATOMIC_RELAXED, __HIP_MEMORY_SCOPE_AGENT); }
; __device__ __forceinline__ void xcd_barrier_complete(unsigned* bar, unsigned x, unsigned& nloc, unsigned& nx) {
;     ...
;     for (;;) {
;         sum = 0u; cnt = 0u;
; #pragma unroll 1
;         for (unsigned j = 0; j < 16; ++j) { const unsigned c = xb_ld(&bar[XB_XCNT(j)]); sum += c; cnt += (c > 0u) ? 1u : 0u; }
;         if (sum == G) break;
;         __builtin_amdgcn_s_sleep(1);
;         if ((++sp & 255u) == 0u) { if (xb_ld(&bar[XB_TMO])) break; if (sp > XB_SPIN_CAP) { (void)xb_add(&bar[XB_TMO], 1u); break; } }
;     }
.LBB0_435:
	s_add_u32 s8, s15, s6
	s_addc_u32 s9, s16, s7
	global_load_dword v3, v35, s[8:9] sc1
	s_waitcnt vmcnt(0)
	v_cmp_ne_u32_e32 vcc, 0, v3
	s_cmp_lg_u64 vcc, 0
	s_addc_u32 s13, s13, 0
	s_add_u32 s6, s6, 0x100
	s_addc_u32 s7, s7, 0
	s_cmpk_eq_i32 s6, 0x1000
	v_add_u32_e32 v2, v3, v2
	s_cbranch_scc0 .LBB0_435
	v_cmp_ne_u32_e32 vcc, s14, v2
	s_mov_b64 s[6:7], -1
	s_mov_b64 s[8:9], -1
	s_cbranch_vccz .LBB0_433
	s_add_i32 s17, s17, 1
	s_and_b32 s8, s17, 0xff
	s_cmp_eq_u32 s8, 0
	s_cselect_b64 s[8:9], -1, 0
	s_and_b64 vcc, exec, s[8:9]
	s_nop 0
	s_cbranch_vccz .LBB0_433
	s_mov_b64 s[6:7], s[4:5]
	global_load_dword v2, v35, s[6:7] sc1
	s_mov_b64 s[6:7], -1
	s_waitcnt vmcnt(0)
	v_cmp_eq_u32_e32 vcc, 0, v2
	s_cbranch_vccz .LBB0_433
	s_cmp_gt_u32 s17, 0x40000
	s_mov_b64 s[6:7], 0
	s_cselect_b64 s[8:9], -1, 0
	s_branch .LBB0_433

; __device__ __forceinline__ unsigned xb_ld(unsigned* p)              { unsigned GAS* g = (unsigned GAS*)p; asm volatile("" : "+s"(g)); return __hip_atomic_load(g, __ATOMIC_RELAXED, __HIP_MEMORY_SCOPE_AGENT); }
; #define XB_SPIN(cond, bar) do { unsigned _sp = 0; while (cond) { __builtin_amdgcn_s_sleep(1); \
;     if ((++_sp & 255u) == 0u) { if (xb_ld(&(bar)[XB_TMO])) break; if (_sp > XB_SPIN_CAP) { (void)xb_add(&(bar)[XB_TMO], 1u); break; } } } } while (0)
; __device__ __forceinline__ void xcd_barrier(const XcdBarrier& b) {
;     ...
;             XB_SPIN(xb_ld(&bar[XB_XGEN(b.x)]) == gen, bar);
.LBB0_451:
	s_mov_b64 s[18:19], s[8:9]
	s_waitcnt lgkmcnt(0)
	global_load_dword v3, v35, s[18:19] sc1
	s_or_b64 s[16:17], s[16:17], exec
	s_or_b64 s[14:15], s[14:15], exec
	s_waitcnt vmcnt(0)
	v_cmp_eq_u32_e32 vcc, v3, v2
	s_and_saveexec_b64 s[18:19], vcc
	s_cbranch_execz .LBB0_450
	s_and_b32 s22, s29, 0xff
	s_mov_b64 s[20:21], -1
	s_cmp_eq_u32 s22, 0
	s_mov_b64 s[22:23], -1
	s_mov_b64 s[24:25], -1
	s_nop 0
	s_cbranch_scc1 .LBB0_455
	s_and_b64 vcc, exec, s[24:25]
	s_cbranch_vccz .LBB0_449

; __device__ __forceinline__ unsigned xb_ld(unsigned* p)              { unsigned GAS* g = (unsigned GAS*)p; asm volatile("" : "+s"(g)); return __hip_atomic_load(g, __ATOMIC_RELAXED, __HIP_MEMORY_SCOPE_AGENT); }
; #define XB_SPIN(cond, bar) do { unsigned _sp = 0; while (cond) { __builtin_amdgcn_s_sleep(1); \
;     if ((++_sp & 255u) == 0u) { if (xb_ld(&(bar)[XB_TMO])) break; if (_sp > XB_SPIN_CAP) { (void)xb_add(&(bar)[XB_TMO], 1u); break; } } } } while (0)
; __device__ __forceinline__ void xcd_barrier(const XcdBarrier& b) {
;     ...
;             else XB_SPIN(xb_ld(&bar[XB_TOPGEN]) == tg, bar);
.LBB0_470:
	s_mov_b64 s[16:17], s[4:5]
	global_load_dword v3, v35, s[16:17] sc1
	s_or_b64 s[14:15], s[14:15], exec
	s_or_b64 s[12:13], s[12:13], exec
	s_waitcnt vmcnt(0)
	v_cmp_eq_u32_e32 vcc, v3, v2
	s_and_saveexec_b64 s[16:17], vcc
	s_cbranch_execz .LBB0_469
	s_and_b32 s20, s24, 0xff
	s_mov_b64 s[18:19], -1
	s_cmp_eq_u32 s20, 0
	s_mov_b64 s[20:21], -1
	s_mov_b64 s[22:23], -1
	s_nop 0
	s_cbranch_scc1 .LBB0_474
	s_and_b64 vcc, exec, s[22:23]
	s_cbranch_vccz .LBB0_468

; __device__ __forceinline__ unsigned xb_ld(unsigned* p)              { unsigned GAS* g = (unsigned GAS*)p; asm volatile("" : "+s"(g)); return __hip_atomic_load(g, __ATOMIC_RELAXED, __HIP_MEMORY_SCOPE_AGENT); }
; __device__ __forceinline__ unsigned xb_add(unsigned* p, unsigned v) { unsigned GAS* g = (unsigned GAS*)p; asm volatile("" : "+s"(g)); return __hip_atomic_fetch_add(g, v, __ATOMIC_RELAXED, __HIP_MEMORY_SCOPE_AGENT); }
; __device__ __forceinline__ void xcd_barrier_complete(unsigned* bar, unsigned x, unsigned& nloc, unsigned& nx) {
;     ...
;     for (;;) {
;         sum = 0u; cnt = 0u;
; #pragma unroll 1
;         for (unsigned j = 0; j < 16; ++j) { const unsigned c = xb_ld(&bar[XB_XCNT(j)]); sum += c; cnt += (c > 0u) ? 1u : 0u; }
;         if (sum == G) break;
;         __builtin_amdgcn_s_sleep(1);
;         if ((++sp & 255u) == 0u) { if (xb_ld(&bar[XB_TMO])) break; if (sp > XB_SPIN_CAP) { (void)xb_add(&bar[XB_TMO], 1u); break; } }
;     }
.LBB0_1036:
	s_add_u32 s8, s15, s6
	s_addc_u32 s9, s16, s7
	global_load_dword v3, v35, s[8:9] sc1
	s_waitcnt vmcnt(0)
	v_cmp_ne_u32_e32 vcc, 0, v3
	s_cmp_lg_u64 vcc, 0
	s_addc_u32 s10, s10, 0
	s_add_u32 s6, s6, 0x100
	s_addc_u32 s7, s7, 0
	s_cmpk_eq_i32 s6, 0x1000
	v_add_u32_e32 v2, v3, v2
	s_cbranch_scc0 .LBB0_1036
	v_cmp_ne_u32_e32 vcc, s14, v2
	s_mov_b64 s[6:7], -1
	s_mov_b64 s[8:9], -1
	s_cbranch_vccz .LBB0_1034
	s_add_i32 s17, s17, 1
	s_and_b32 s8, s17, 0xff
	s_cmp_eq_u32 s8, 0
	s_cselect_b64 s[8:9], -1, 0
	s_and_b64 vcc, exec, s[8:9]
	s_nop 0
	s_cbranch_vccz .LBB0_1034
	s_mov_b64 s[6:7], s[4:5]
	global_load_dword v2, v35, s[6:7] sc1
	s_mov_b64 s[6:7], -1
	s_waitcnt vmcnt(0)
	v_cmp_eq_u32_e32 vcc, 0, v2
	s_cbranch_vccz .LBB0_1034
	s_cmp_gt_u32 s17, 0x40000
	s_mov_b64 s[6:7], 0
	s_cselect_b64 s[8:9], -1, 0
	s_branch .LBB0_1034

; __device__ __forceinline__ unsigned xb_ld(unsigned* p)              { unsigned GAS* g = (unsigned GAS*)p; asm volatile("" : "+s"(g)); return __hip_atomic_load(g, __ATOMIC_RELAXED, __HIP_MEMORY_SCOPE_AGENT); }
; __device__ __forceinline__ unsigned xb_add(unsigned* p, unsigned v) { unsigned GAS* g = (unsigned GAS*)p; asm volatile("" : "+s"(g)); return __hip_atomic_fetch_add(g, v, __ATOMIC_RELAXED, __HIP_MEMORY_SCOPE_AGENT); }
; __device__ __forceinline__ void xcd_barrier_complete(unsigned* bar, unsigned x, unsigned& nloc, unsigned& nx) {
;     ...
;     for (;;) {
;         sum = 0u; cnt = 0u;
; #pragma unroll 1
;         for (unsigned j = 0; j < 16; ++j) { const unsigned c = xb_ld(&bar[XB_XCNT(j)]); sum += c; cnt += (c > 0u) ? 1u : 0u; }
;         if (sum == G) break;
;         __builtin_amdgcn_s_sleep(1);
;         if ((++sp & 255u) == 0u) { if (xb_ld(&bar[XB_TMO])) break; if (sp > XB_SPIN_CAP) { (void)xb_add(&bar[XB_TMO], 1u); break; } }
;     }
.LBB0_1432:
	s_add_u32 s10, s17, s6
	s_addc_u32 s11, s18, s7
	global_load_dword v3, v35, s[10:11] sc1
	s_waitcnt vmcnt(0)
	v_cmp_ne_u32_e32 vcc, 0, v3
	s_cmp_lg_u64 vcc, 0
	s_addc_u32 s15, s15, 0
	s_add_u32 s6, s6, 0x100
	s_addc_u32 s7, s7, 0
	s_cmpk_eq_i32 s6, 0x1000
	v_add_u32_e32 v2, v3, v2
	s_cbranch_scc0 .LBB0_1432
	v_cmp_ne_u32_e32 vcc, s16, v2
	s_mov_b64 s[6:7], -1
	s_mov_b64 s[10:11], -1
	s_cbranch_vccz .LBB0_1430
	s_add_i32 s19, s19, 1
	s_and_b32 s10, s19, 0xff
	s_cmp_eq_u32 s10, 0
	s_cselect_b64 s[10:11], -1, 0
	s_and_b64 vcc, exec, s[10:11]
	s_nop 0
	s_cbranch_vccz .LBB0_1430
	s_mov_b64 s[6:7], s[4:5]
	global_load_dword v2, v35, s[6:7] sc1
	s_mov_b64 s[6:7], -1
	s_waitcnt vmcnt(0)
	v_cmp_eq_u32_e32 vcc, 0, v2
	s_cbranch_vccz .LBB0_1430
	s_cmp_gt_u32 s19, 0x40000
	s_mov_b64 s[6:7], 0
	s_cselect_b64 s[10:11], -1, 0
	s_branch .LBB0_1430

; __device__ __forceinline__ unsigned xb_ld(unsigned* p)              { unsigned GAS* g = (unsigned GAS*)p; asm volatile("" : "+s"(g)); return __hip_atomic_load(g, __ATOMIC_RELAXED, __HIP_MEMORY_SCOPE_AGENT); }
; #define XB_SPIN(cond, bar) do { unsigned _sp = 0; while (cond) { __builtin_amdgcn_s_sleep(1); \
;     if ((++_sp & 255u) == 0u) { if (xb_ld(&(bar)[XB_TMO])) break; if (_sp > XB_SPIN_CAP) { (void)xb_add(&(bar)[XB_TMO], 1u); break; } } } } while (0)
; __device__ __forceinline__ void xcd_barrier(const XcdBarrier& b) {
;     ...
;             XB_SPIN(xb_ld(&bar[XB_XGEN(b.x)]) == gen, bar);
.LBB0_1448:
	s_mov_b64 s[20:21], s[10:11]
	s_waitcnt lgkmcnt(0)
	global_load_dword v3, v35, s[20:21] sc1
	s_or_b64 s[18:19], s[18:19], exec
	s_or_b64 s[16:17], s[16:17], exec
	s_waitcnt vmcnt(0)
	v_cmp_eq_u32_e32 vcc, v3, v2
	s_and_saveexec_b64 s[20:21], vcc
	s_cbranch_execz .LBB0_1447
	s_and_b32 s24, s31, 0xff
	s_mov_b64 s[22:23], -1
	s_cmp_eq_u32 s24, 0
	s_mov_b64 s[24:25], -1
	s_mov_b64 s[26:27], -1
	s_nop 0
	s_cbranch_scc1 .LBB0_1452
	s_and_b64 vcc, exec, s[26:27]
	s_cbranch_vccz .LBB0_1446

; __device__ __forceinline__ unsigned xb_ld(unsigned* p)              { unsigned GAS* g = (unsigned GAS*)p; asm volatile("" : "+s"(g)); return __hip_atomic_load(g, __ATOMIC_RELAXED, __HIP_MEMORY_SCOPE_AGENT); }
; #define XB_SPIN(cond, bar) do { unsigned _sp = 0; while (cond) { __builtin_amdgcn_s_sleep(1); \
;     if ((++_sp & 255u) == 0u) { if (xb_ld(&(bar)[XB_TMO])) break; if (_sp > XB_SPIN_CAP) { (void)xb_add(&(bar)[XB_TMO], 1u); break; } } } } while (0)
; __device__ __forceinline__ void xcd_barrier(const XcdBarrier& b) {
;     ...
;             else XB_SPIN(xb_ld(&bar[XB_TOPGEN]) == tg, bar);
.LBB0_1467:
	s_mov_b64 s[18:19], s[4:5]
	global_load_dword v3, v35, s[18:19] sc1
	s_or_b64 s[16:17], s[16:17], exec
	s_or_b64 s[14:15], s[14:15], exec
	s_waitcnt vmcnt(0)
	v_cmp_eq_u32_e32 vcc, v3, v2
	s_and_saveexec_b64 s[18:19], vcc
	s_cbranch_execz .LBB0_1466
	s_and_b32 s22, s26, 0xff
	s_mov_b64 s[20:21], -1
	s_cmp_eq_u32 s22, 0
	s_mov_b64 s[22:23], -1
	s_mov_b64 s[24:25], -1
	s_nop 0
	s_cbranch_scc1 .LBB0_1471
	s_and_b64 vcc, exec, s[24:25]
	s_cbranch_vccz .LBB0_1465

; __device__ __forceinline__ unsigned xb_ld(unsigned* p)              { unsigned GAS* g = (unsigned GAS*)p; asm volatile("" : "+s"(g)); return __hip_atomic_load(g, __ATOMIC_RELAXED, __HIP_MEMORY_SCOPE_AGENT); }
; #define XB_SPIN(cond, bar) do { unsigned _sp = 0; while (cond) { __builtin_amdgcn_s_sleep(1); \
;     if ((++_sp & 255u) == 0u) { if (xb_ld(&(bar)[XB_TMO])) break; if (_sp > XB_SPIN_CAP) { (void)xb_add(&(bar)[XB_TMO], 1u); break; } } } } while (0)
; __device__ __forceinline__ void xcd_barrier(const XcdBarrier& b) {
;     ...
;             XB_SPIN(xb_ld(&bar[XB_XGEN(b.x)]) == gen, bar);
.LBB0_1541:
	s_mov_b64 s[18:19], s[8:9]
	s_waitcnt lgkmcnt(0)
	global_load_dword v3, v35, s[18:19] sc1
	s_or_b64 s[16:17], s[16:17], exec
	s_or_b64 s[14:15], s[14:15], exec
	s_waitcnt vmcnt(0)
	v_cmp_eq_u32_e32 vcc, v3, v2
	s_and_saveexec_b64 s[18:19], vcc
	s_cbranch_execz .LBB0_1540
	s_and_b32 s22, s28, 0xff
	s_mov_b64 s[20:21], -1
	s_cmp_eq_u32 s22, 0
	s_mov_b64 s[22:23], -1
	s_mov_b64 s[24:25], -1
	s_nop 0
	s_cbranch_scc1 .LBB0_1545
	s_and_b64 vcc, exec, s[24:25]
	s_cbranch_vccz .LBB0_1539
